# baseline (speedup 1.0000x reference)
.Lp_next:
	s_waitcnt lgkmcnt(4)
.Lp_top:
	s_setprio 2
	s_cmp_eq_u32 s52, 1
	s_cbranch_scc1 .Lp_done
	v_readfirstlane_b32 s35, v12
	v_readfirstlane_b32 s36, v13
	s_nop 1
	v_mov_b32_e32 v10, s35
	v_mov_b32_e32 v11, s36
	v_cndmask_b32_e64 v12, v10, v11, s[54:55]
	v_cndmask_b32_e64 v13, v10, v11, s[56:57]
	v_lshl_add_u32 v12, v12, 3, v61
	v_lshl_add_u32 v14, v13, 4, v62
	ds_read_b64 v[2:3], v12
	ds_read_b128 v[4:7], v14
	v_mad_u32_u24 v9, v13, s49, v58
	v_mov_b32_e32 v8, v56
	s_waitcnt lgkmcnt(0)
	v_add_u32_e32 v2, v2, v55
	v_and_b32_e32 v3, v3, v63
	s_nop 0
	v_readlane_b32 s41, v3, 0
	v_readlane_b32 s42, v3, 4
	s_max_u32 s43, s41, s42
	s_cmp_eq_u32 s43, 0
	s_cbranch_scc1 .Lp_zero
	ds_read_b64 v[36:37], v2
	v_cmp_gt_u32_e32 vcc, v3, v8
	v_add_u32_e32 v2, 64, v2
	v_add_u32_e32 v8, 16, v8
	v_mov_b32_e32 v33, 0x3c00
	s_waitcnt lgkmcnt(0)
	v_perm_b32 v32, v37, v36, v57
	v_cndmask_b32_e32 v33, 0, v33, vcc
	s_nop 0
	v_cndmask_b32_e32 v32, 0, v32, vcc
	s_nop 1
	v_mfma_f32_32x32x16_f16 v[96:111], v[32:35], v[64:67], 0
	v_mfma_f32_32x32x16_f16 v[112:127], v[32:35], v[68:71], 0
	s_setprio 0
	s_nop 10
	s_mov_b32 s45, s43
	s_min_u32 s46, s45, 16
	s_cmp_eq_u32 s46, 16
	s_cbranch_scc1 .Lf16
	s_cmp_eq_u32 s46, 15
	s_cbranch_scc1 .Lf15
	s_cmp_eq_u32 s46, 14
	s_cbranch_scc1 .Lf14
	s_cmp_eq_u32 s46, 13
	s_cbranch_scc1 .Lf13
	s_cmp_eq_u32 s46, 12
	s_cbranch_scc1 .Lf12
	s_cmp_eq_u32 s46, 11
	s_cbranch_scc1 .Lf11
	s_cmp_eq_u32 s46, 10
	s_cbranch_scc1 .Lf10
	s_cmp_eq_u32 s46, 9
	s_cbranch_scc1 .Lf9
	s_cmp_eq_u32 s46, 8
	s_cbranch_scc1 .Lf8
	s_cmp_eq_u32 s46, 7
	s_cbranch_scc1 .Lf7
	s_cmp_eq_u32 s46, 6
	s_cbranch_scc1 .Lf6
	s_cmp_eq_u32 s46, 5
	s_cbranch_scc1 .Lf5
	s_cmp_eq_u32 s46, 4
	s_cbranch_scc1 .Lf4
	s_cmp_eq_u32 s46, 3
	s_cbranch_scc1 .Lf3
	s_cmp_eq_u32 s46, 2
	s_cbranch_scc1 .Lf2

.Lp_fin:
	s_setprio 2
	s_mov_b64 exec, 1
	ds_add_rtn_u32 v10, v59, v60
	s_mov_b64 exec, -1
	v_mul_f32_e32 v40, v7, v24
	v_fma_mix_f32 v40, v6, v65, v40 op_sel_hi:[0,1,0]
	v_fma_mix_f32 v40, v5, v64, v40 op_sel:[0,1,0] op_sel_hi:[0,1,0]
	v_fma_mixlo_f16 v40, v4, v64, v40 op_sel_hi:[0,1,0]
	ds_write_b16 v9, v40 offset:0
	v_mul_f32_e32 v41, v7, v25
	v_fma_mix_f32 v41, v6, v69, v41 op_sel_hi:[0,1,0]
	v_fma_mix_f32 v41, v5, v68, v41 op_sel:[0,1,0] op_sel_hi:[0,1,0]
	v_fma_mixlo_f16 v41, v4, v68, v41 op_sel_hi:[0,1,0]
	ds_write_b16 v9, v41 offset:64
	v_mul_f32_e32 v40, v7, v26
	v_fma_mix_f32 v40, v6, v73, v40 op_sel_hi:[0,1,0]
	v_fma_mix_f32 v40, v5, v72, v40 op_sel:[0,1,0] op_sel_hi:[0,1,0]
	v_fma_mixlo_f16 v40, v4, v72, v40 op_sel_hi:[0,1,0]
	ds_write_b16 v9, v40 offset:128
	v_mul_f32_e32 v41, v7, v27
	v_fma_mix_f32 v41, v6, v77, v41 op_sel_hi:[0,1,0]
	v_fma_mix_f32 v41, v5, v76, v41 op_sel:[0,1,0] op_sel_hi:[0,1,0]
	v_fma_mixlo_f16 v41, v4, v76, v41 op_sel_hi:[0,1,0]
	ds_write_b16 v9, v41 offset:192
	s_waitcnt lgkmcnt(4)
	v_readfirstlane_b32 s34, v10
	s_cmp_lt_u32 s34, s62
	s_cselect_b32 s45, s64, s65
	s_cselect_b32 s46, 0, s62
	s_cselect_b32 s48, s62, s63
	s_sub_u32 s47, s34, s46
	s_cmp_ge_u32 s47, s48
	s_cselect_b32 s52, 1, 0
	s_lshl_b32 s47, s47, 3
	s_add_u32 s45, s45, s47
	v_mov_b32_e32 v11, s45
	ds_read2_b32 v[12:13], v11 offset1:1
	v_mul_f32_e32 v40, v7, v28
	v_fma_mix_f32 v40, v6, v81, v40 op_sel_hi:[0,1,0]
	v_fma_mix_f32 v40, v5, v80, v40 op_sel:[0,1,0] op_sel_hi:[0,1,0]
	v_fma_mixlo_f16 v40, v4, v80, v40 op_sel_hi:[0,1,0]
	ds_write_b16 v9, v40 offset:256
	v_mul_f32_e32 v41, v7, v29
	v_fma_mix_f32 v41, v6, v85, v41 op_sel_hi:[0,1,0]
	v_fma_mix_f32 v41, v5, v84, v41 op_sel:[0,1,0] op_sel_hi:[0,1,0]
	v_fma_mixlo_f16 v41, v4, v84, v41 op_sel_hi:[0,1,0]
	ds_write_b16 v9, v41 offset:320
	v_mul_f32_e32 v40, v7, v30
	v_fma_mix_f32 v40, v6, v89, v40 op_sel_hi:[0,1,0]
	v_fma_mix_f32 v40, v5, v88, v40 op_sel:[0,1,0] op_sel_hi:[0,1,0]
	v_fma_mixlo_f16 v40, v4, v88, v40 op_sel_hi:[0,1,0]
	ds_write_b16 v9, v40 offset:384
	v_mul_f32_e32 v41, v7, v31
	v_fma_mix_f32 v41, v6, v93, v41 op_sel_hi:[0,1,0]
	v_fma_mix_f32 v41, v5, v92, v41 op_sel:[0,1,0] op_sel_hi:[0,1,0]
	v_fma_mixlo_f16 v41, v4, v92, v41 op_sel_hi:[0,1,0]
	ds_write_b16 v9, v41 offset:448
	s_branch .Lp_next
